# gemm_in: asymmetric final rendezvous - waves 4-7 run their epilogue before the K-loop's final barrier, waves 0-3 after it (epilogues overlap instead of serializing)
# speedup vs baseline: 1.0048x; 1.0042x over previous
; template <class Epi, class Sched>
; __device__ __forceinline__ void gemm_phase(LAS unsigned char* lds, const bf16_t* Abase, const int K, const Sched& S, const Epi& E, const int wvid) {
;     ...
;         E(acc, cur, wr, wc, fr, fq);
;         if (!has_next) break;
; #pragma unroll
;         for (int a = 0; a < 2; ++a)
; #pragma unroll
;             for (int b = 0; b < 2; ++b)
; #pragma unroll
;                 for (int m = 0; m < 4; ++m)
; #pragma unroll
;                     for (int n = 0; n < 2; ++n) acc[a][b][m][n] = (f32x4){0.f, 0.f, 0.f, 0.f};
;         cur = nxt; cB = nB; ++ui;
;     }
.LBB0_117:
	s_or_b64 exec, exec, s[28:29]
	s_cmp_lt_u32 s74, 0x100
	s_cbranch_scc1 .Ly_in
	s_barrier
.Ly_in:
	s_and_b64 vcc, exec, s[2:3]
	s_mov_b32 s57, s56
	s_mov_b32 s16, s24
	s_mov_b64 s[4:5], s[26:27]
	s_cbranch_vccnz .LBB0_202

; #define PG8_STAGE(bufoff, gbase, voff) do { _Pragma("unroll") for (int _i = 0; _i < 2; ++_i) \
;         __builtin_amdgcn_global_load_lds((const unsigned*)((const char*)(gbase) + (voff)[_i]), (LAS unsigned*)(lds + (bufoff) + ldsw + _i * 8192), 16, 0, 0); } while (0)
; #define PG8_LDA(dst, b, h) do { _Pragma("unroll") for (int m = 0; m < 4; ++m) _Pragma("unroll") for (int k = 0; k < 2; ++k) dst[m][k] = *(const LAS bf16x8*)(lds + PG8_SA(b, h) + aoff + m * 2048 + k * 1024); } while (0)
; #define PG8_LDB(dst, b, h) do { _Pragma("unroll") for (int n = 0; n < 2; ++n) _Pragma("unroll") for (int k = 0; k < 2; ++k) dst[n][k] = *(const LAS bf16x8*)(lds + PG8_SB(b, h) + boff + n * 2048 + k * 1024); } while (0)
; #define PG8_MMA(ai, bj, At, Bt) do { __builtin_amdgcn_s_setprio(1); _Pragma("unroll") for (int m = 0; m < 4; ++m) _Pragma("unroll") for (int n = 0; n < 2; ++n) _Pragma("unroll") for (int k = 0; k < 2; ++k) \
;         acc[ai][bj][m][n] = __builtin_amdgcn_mfma_f32_16x16x32_bf16(Bt[n][k], At[m][k], acc[ai][bj][m][n], 0, 0, 0); __builtin_amdgcn_s_setprio(0); } while (0)
; #define PG8_WAIT_V(n) asm volatile("s_waitcnt vmcnt(" #n ")" ::: "memory")
; #define PG8_WAIT_L(n) asm volatile("s_waitcnt lgkmcnt(" #n ")" ::: "memory")
; #define PG8_BAR __builtin_amdgcn_s_barrier()
; #define PG8_SCHED __builtin_amdgcn_sched_barrier(0)
; template <class Epi, class Sched>
; __device__ __forceinline__ void gemm_phase(LAS unsigned char* lds, const bf16_t* Abase, const int K, const Sched& S, const Epi& E, const int wvid) {
;     ...
;             PG8_LDB(B0, 0, 0); PG8_SCHED; PG8_LDA(At, 0, 0); PG8_STAGE(PG8_SA(1, 1), a1, voffA[1]);
;             PG8_WAIT_L(8); PG8_BAR; PG8_WAIT_L(0); PG8_MMA(0, 0, At, B0); PG8_BAR; PG8_SCHED;
;             if (last && has_next) PG8_AOFF(nxt);
;             const char* a2 = last ? Ab : Ab + (size_t)(t + 2) * kstep; const char* b2 = last ? nB : cB + (size_t)(t + 2) * kstep;
;             const char* a3 = a2 + kstep; const char* b3 = b2 + kstep;
;             PG8_LDB(B1, 0, 1); PG8_STAGE(PG8_SB(0, 0), b2, voffB);
;             PG8_BAR; PG8_WAIT_L(0); PG8_MMA(0, 1, At, B1); PG8_BAR;
;             PG8_LDA(At, 0, 1); PG8_STAGE(PG8_SA(0, 0), a2, voffA[0]);
;             PG8_BAR; PG8_WAIT_L(0); PG8_MMA(1, 0, At, B0); PG8_BAR; PG8_SCHED;
;             PG8_STAGE(PG8_SB(0, 1), b2 + hstep, voffB);
;             PG8_WAIT_V(6); PG8_BAR; PG8_MMA(1, 1, At, B1); PG8_BAR;
.LBB0_128:
	s_add_u32 s28, s4, 0x100
	s_addc_u32 s29, s5, 0
	s_and_b64 s[34:35], s[30:31], exec
	s_cselect_b32 s34, 0, s28
	s_cselect_b32 s35, 0, s29
	s_add_u32 s34, s10, s34
	s_addc_u32 s35, s11, s35
	s_add_u32 s62, s59, s4
	s_addc_u32 s63, s60, s5
	s_add_i32 s64, 0, 0x14000
	s_and_b64 s[4:5], s[30:31], exec
	s_cselect_b32 s5, s25, s63
	s_cselect_b32 s4, s58, s62
	s_mov_b32 m0, s42
	v_add_u32_e32 v183, s64, v192
	v_lshl_add_u64 v[200:201], s[4:5], 0, v[178:179]
	ds_read_b128 v[196:199], v183
	ds_read_b128 v[224:227], v183 offset:1024
	ds_read_b128 v[228:231], v183 offset:2048
	ds_read_b128 v[232:235], v183 offset:3072
	global_load_lds_dwordx4 v[200:201], off
	v_lshl_add_u64 v[202:203], s[4:5], 0, v[180:181]
	s_mov_b32 m0, s43
	s_nop 0
	global_load_lds_dwordx4 v[202:203], off
	s_barrier
	s_waitcnt lgkmcnt(0)
	s_waitcnt lgkmcnt(0)
	v_mfma_f32_16x16x32_bf16 v[110:113], v[196:199], v[170:173], v[110:113]
	v_mfma_f32_16x16x32_bf16 v[106:109], v[228:231], v[170:173], v[106:109]
	v_mfma_f32_16x16x32_bf16 v[94:97], v[196:199], v[162:165], v[94:97]
	v_mfma_f32_16x16x32_bf16 v[90:93], v[228:231], v[162:165], v[90:93]
	v_mfma_f32_16x16x32_bf16 v[78:81], v[196:199], v[154:157], v[78:81]
	v_mfma_f32_16x16x32_bf16 v[74:77], v[228:231], v[154:157], v[74:77]
	v_mfma_f32_16x16x32_bf16 v[70:73], v[196:199], v[146:149], v[70:73]
	v_mfma_f32_16x16x32_bf16 v[66:69], v[228:231], v[146:149], v[66:69]
	v_mfma_f32_16x16x32_bf16 v[110:113], v[224:227], v[174:177], v[110:113]
	v_mfma_f32_16x16x32_bf16 v[106:109], v[232:235], v[174:177], v[106:109]
	v_mfma_f32_16x16x32_bf16 v[94:97], v[224:227], v[166:169], v[94:97]
	v_mfma_f32_16x16x32_bf16 v[90:93], v[232:235], v[166:169], v[90:93]
	v_mfma_f32_16x16x32_bf16 v[78:81], v[224:227], v[158:161], v[78:81]
	v_mfma_f32_16x16x32_bf16 v[74:77], v[232:235], v[158:161], v[74:77]
	v_mfma_f32_16x16x32_bf16 v[70:73], v[224:227], v[150:153], v[70:73]
	v_mfma_f32_16x16x32_bf16 v[66:69], v[232:235], v[150:153], v[66:69]
	s_mov_b32 m0, s17
	s_barrier
	ds_read_b128 v[146:149], v194 offset:16384
	ds_read_b128 v[150:153], v194 offset:17408
	ds_read_b128 v[154:157], v194 offset:18432
	ds_read_b128 v[158:161], v194 offset:19456
	ds_read_b128 v[162:165], v194 offset:20480
	ds_read_b128 v[166:169], v194 offset:21504
	ds_read_b128 v[170:173], v194 offset:22528
	ds_read_b128 v[174:177], v194 offset:23552
	global_load_lds_dwordx4 v0, s[34:35]
	s_mov_b32 m0, s46
	v_mov_b32_e32 v185, v1
	global_load_lds_dwordx4 v184, s[34:35]
	s_barrier
	s_waitcnt lgkmcnt(0)
	v_lshl_add_u64 v[206:207], s[34:35], 0, v[0:1]
	v_lshl_add_u64 v[208:209], s[34:35], 0, v[184:185]
	s_waitcnt lgkmcnt(0)
	v_mfma_f32_16x16x32_bf16 v[62:65], v[130:133], v[146:149], v[62:65]
	v_mfma_f32_16x16x32_bf16 v[58:61], v[138:141], v[146:149], v[58:61]
	v_mfma_f32_16x16x32_bf16 v[46:49], v[130:133], v[154:157], v[46:49]
	v_mfma_f32_16x16x32_bf16 v[42:45], v[138:141], v[154:157], v[42:45]
	v_mfma_f32_16x16x32_bf16 v[30:33], v[130:133], v[162:165], v[30:33]
	v_mfma_f32_16x16x32_bf16 v[26:29], v[138:141], v[162:165], v[26:29]
	v_mfma_f32_16x16x32_bf16 v[14:17], v[130:133], v[170:173], v[14:17]
	v_mfma_f32_16x16x32_bf16 v[10:13], v[138:141], v[170:173], v[10:13]
	v_mfma_f32_16x16x32_bf16 v[62:65], v[134:137], v[150:153], v[62:65]
	v_mfma_f32_16x16x32_bf16 v[58:61], v[142:145], v[150:153], v[58:61]
	v_mfma_f32_16x16x32_bf16 v[46:49], v[134:137], v[158:161], v[46:49]
	v_mfma_f32_16x16x32_bf16 v[42:45], v[142:145], v[158:161], v[42:45]
	v_mfma_f32_16x16x32_bf16 v[30:33], v[134:137], v[166:169], v[30:33]
	v_mfma_f32_16x16x32_bf16 v[26:29], v[142:145], v[166:169], v[26:29]
	v_mfma_f32_16x16x32_bf16 v[14:17], v[134:137], v[174:177], v[14:17]
	v_mfma_f32_16x16x32_bf16 v[10:13], v[142:145], v[174:177], v[10:13]
	s_barrier
	s_add_u32 s30, s4, 0x40000
	s_addc_u32 s31, s5, 0
	s_add_i32 s62, s64, s40
	v_lshl_add_u64 v[130:131], s[30:31], 0, v[178:179]
	s_mov_b32 m0, s62
	s_nop 0
	global_load_lds_dwordx4 v[130:131], off
	v_lshl_add_u64 v[130:131], s[30:31], 0, v[180:181]
	s_add_i32 m0, s62, 0x2000
	s_nop 0
	global_load_lds_dwordx4 v[130:131], off
	s_waitcnt vmcnt(6)
	s_barrier
	v_mfma_f32_16x16x32_bf16 v[54:57], v[196:199], v[146:149], v[54:57]
	v_mfma_f32_16x16x32_bf16 v[50:53], v[228:231], v[146:149], v[50:53]
	v_mfma_f32_16x16x32_bf16 v[38:41], v[196:199], v[154:157], v[38:41]
	v_mfma_f32_16x16x32_bf16 v[34:37], v[228:231], v[154:157], v[34:37]
	v_mfma_f32_16x16x32_bf16 v[22:25], v[196:199], v[162:165], v[22:25]
	v_mfma_f32_16x16x32_bf16 v[18:21], v[228:231], v[162:165], v[18:21]
	v_mfma_f32_16x16x32_bf16 v[6:9], v[196:199], v[170:173], v[6:9]
	v_mfma_f32_16x16x32_bf16 v[2:5], v[228:231], v[170:173], v[2:5]
	v_mfma_f32_16x16x32_bf16 v[54:57], v[224:227], v[150:153], v[54:57]
	v_mfma_f32_16x16x32_bf16 v[50:53], v[232:235], v[150:153], v[50:53]
	v_mfma_f32_16x16x32_bf16 v[38:41], v[224:227], v[158:161], v[38:41]
	v_mfma_f32_16x16x32_bf16 v[34:37], v[232:235], v[158:161], v[34:37]
	v_mfma_f32_16x16x32_bf16 v[22:25], v[224:227], v[166:169], v[22:25]
	v_mfma_f32_16x16x32_bf16 v[18:21], v[232:235], v[166:169], v[18:21]
	v_mfma_f32_16x16x32_bf16 v[6:9], v[224:227], v[174:177], v[6:9]
	v_mfma_f32_16x16x32_bf16 v[2:5], v[232:235], v[174:177], v[2:5]
	s_add_i32 s30, 0, 0x18000
	v_add_u32_e32 v142, s30, v192
	s_barrier
	ds_read_b128 v[130:133], v142
	ds_read_b128 v[134:137], v142 offset:1024
	ds_read_b128 v[138:141], v142 offset:2048
	ds_read_b128 v[142:145], v142 offset:3072
	s_mov_b32 m0, s47
	v_lshl_add_u64 v[188:189], s[34:35], 0, v[188:189]
	ds_read_b128 v[146:149], v194 offset:32768
	ds_read_b128 v[150:153], v194 offset:33792
	ds_read_b128 v[154:157], v194 offset:34816
	ds_read_b128 v[158:161], v194 offset:35840
	ds_read_b128 v[162:165], v194 offset:36864
	ds_read_b128 v[166:169], v194 offset:37888
	ds_read_b128 v[170:173], v194 offset:38912
	ds_read_b128 v[174:177], v194 offset:39936
	global_load_lds_dwordx4 v[188:189], off
	v_lshl_add_u64 v[188:189], s[34:35], 0, v[186:187]
	s_mov_b32 m0, s48
	s_nop 0
	global_load_lds_dwordx4 v[188:189], off
	s_waitcnt lgkmcnt(8)
	s_barrier
; #define PG8_STAGE(bufoff, gbase, voff) do { _Pragma("unroll") for (int _i = 0; _i < 2; ++_i) \
;         __builtin_amdgcn_global_load_lds((const unsigned*)((const char*)(gbase) + (voff)[_i]), (LAS unsigned*)(lds + (bufoff) + ldsw + _i * 8192), 16, 0, 0); } while (0)
; #define PG8_LDA(dst, b, h) do { _Pragma("unroll") for (int m = 0; m < 4; ++m) _Pragma("unroll") for (int k = 0; k < 2; ++k) dst[m][k] = *(const LAS bf16x8*)(lds + PG8_SA(b, h) + aoff + m * 2048 + k * 1024); } while (0)
; #define PG8_LDB(dst, b, h) do { _Pragma("unroll") for (int n = 0; n < 2; ++n) _Pragma("unroll") for (int k = 0; k < 2; ++k) dst[n][k] = *(const LAS bf16x8*)(lds + PG8_SB(b, h) + boff + n * 2048 + k * 1024); } while (0)
; #define PG8_MMA(ai, bj, At, Bt) do { __builtin_amdgcn_s_setprio(1); _Pragma("unroll") for (int m = 0; m < 4; ++m) _Pragma("unroll") for (int n = 0; n < 2; ++n) _Pragma("unroll") for (int k = 0; k < 2; ++k) \
;         acc[ai][bj][m][n] = __builtin_amdgcn_mfma_f32_16x16x32_bf16(Bt[n][k], At[m][k], acc[ai][bj][m][n], 0, 0, 0); __builtin_amdgcn_s_setprio(0); } while (0)
; #define PG8_WAIT_V(n) asm volatile("s_waitcnt vmcnt(" #n ")" ::: "memory")
; #define PG8_WAIT_L(n) asm volatile("s_waitcnt lgkmcnt(" #n ")" ::: "memory")
; #define PG8_BAR __builtin_amdgcn_s_barrier()
; #define PG8_SCHED __builtin_amdgcn_sched_barrier(0)
; template <class Epi, class Sched>
; __device__ __forceinline__ void gemm_phase(LAS unsigned char* lds, const bf16_t* Abase, const int K, const Sched& S, const Epi& E, const int wvid) {
;     ...
;             PG8_LDB(B0, 1, 0); PG8_SCHED; PG8_LDA(At, 1, 0); PG8_STAGE(PG8_SA(0, 1), a2, voffA[1]);
;             PG8_WAIT_L(8); PG8_BAR; PG8_WAIT_L(0); PG8_MMA(0, 0, At, B0); PG8_BAR; PG8_SCHED;
;             PG8_LDB(B1, 1, 1); PG8_STAGE(PG8_SB(1, 0), b3, voffB);
;             PG8_BAR; PG8_WAIT_L(0); PG8_MMA(0, 1, At, B1); PG8_BAR;
;             PG8_LDA(At, 1, 1); PG8_STAGE(PG8_SA(1, 0), a3, voffA[0]);
;             PG8_BAR; PG8_WAIT_L(0); PG8_MMA(1, 0, At, B0); PG8_BAR; PG8_SCHED;
;             PG8_STAGE(PG8_SB(1, 1), b3 + hstep, voffB);
;             PG8_WAIT_V(6); PG8_BAR; PG8_MMA(1, 1, At, B1); PG8_BAR;
;         }
	s_waitcnt lgkmcnt(0)
	s_waitcnt lgkmcnt(0)
	v_mfma_f32_16x16x32_bf16 v[126:129], v[130:133], v[146:149], v[126:129]
	v_mfma_f32_16x16x32_bf16 v[122:125], v[138:141], v[146:149], v[122:125]
	v_mfma_f32_16x16x32_bf16 v[118:121], v[130:133], v[154:157], v[118:121]
	v_mfma_f32_16x16x32_bf16 v[114:117], v[138:141], v[154:157], v[114:117]
	v_mfma_f32_16x16x32_bf16 v[102:105], v[130:133], v[162:165], v[102:105]
	v_mfma_f32_16x16x32_bf16 v[98:101], v[138:141], v[162:165], v[98:101]
	v_mfma_f32_16x16x32_bf16 v[86:89], v[130:133], v[170:173], v[86:89]
	v_mfma_f32_16x16x32_bf16 v[82:85], v[138:141], v[170:173], v[82:85]
	v_mfma_f32_16x16x32_bf16 v[126:129], v[134:137], v[150:153], v[126:129]
	v_mfma_f32_16x16x32_bf16 v[122:125], v[142:145], v[150:153], v[122:125]
	v_mfma_f32_16x16x32_bf16 v[118:121], v[134:137], v[158:161], v[118:121]
	v_mfma_f32_16x16x32_bf16 v[114:117], v[142:145], v[158:161], v[114:117]
	v_mfma_f32_16x16x32_bf16 v[102:105], v[134:137], v[166:169], v[102:105]
	v_mfma_f32_16x16x32_bf16 v[98:101], v[142:145], v[166:169], v[98:101]
	v_mfma_f32_16x16x32_bf16 v[86:89], v[134:137], v[174:177], v[86:89]
	v_mfma_f32_16x16x32_bf16 v[82:85], v[142:145], v[174:177], v[82:85]
	s_barrier
	s_add_i32 s31, 0, 0x1c000
	s_add_i32 s30, s30, s40
	v_add_u32_e32 v183, s31, v192
	v_lshl_add_u64 v[188:189], v[200:201], 0, s[12:13]
	s_mov_b32 m0, s30
	ds_read_b128 v[196:199], v183
	ds_read_b128 v[224:227], v183 offset:1024
	ds_read_b128 v[228:231], v183 offset:2048
	ds_read_b128 v[232:235], v183 offset:3072
	global_load_lds_dwordx4 v[188:189], off
	v_lshl_add_u64 v[188:189], v[202:203], 0, s[12:13]
	s_add_i32 m0, s30, 0x2000
	s_nop 0
	global_load_lds_dwordx4 v[188:189], off
	s_barrier
	s_waitcnt lgkmcnt(0)
	s_waitcnt lgkmcnt(0)
	v_mfma_f32_16x16x32_bf16 v[110:113], v[196:199], v[146:149], v[110:113]
	v_mfma_f32_16x16x32_bf16 v[106:109], v[228:231], v[146:149], v[106:109]
	v_mfma_f32_16x16x32_bf16 v[94:97], v[196:199], v[154:157], v[94:97]
	v_mfma_f32_16x16x32_bf16 v[90:93], v[228:231], v[154:157], v[90:93]
	v_mfma_f32_16x16x32_bf16 v[78:81], v[196:199], v[162:165], v[78:81]
	v_mfma_f32_16x16x32_bf16 v[74:77], v[228:231], v[162:165], v[74:77]
	v_mfma_f32_16x16x32_bf16 v[70:73], v[196:199], v[170:173], v[70:73]
	v_mfma_f32_16x16x32_bf16 v[66:69], v[228:231], v[170:173], v[66:69]
	v_mfma_f32_16x16x32_bf16 v[110:113], v[224:227], v[150:153], v[110:113]
	v_mfma_f32_16x16x32_bf16 v[106:109], v[232:235], v[150:153], v[106:109]
	v_mfma_f32_16x16x32_bf16 v[94:97], v[224:227], v[158:161], v[94:97]
	v_mfma_f32_16x16x32_bf16 v[90:93], v[232:235], v[158:161], v[90:93]
	v_mfma_f32_16x16x32_bf16 v[78:81], v[224:227], v[166:169], v[78:81]
	v_mfma_f32_16x16x32_bf16 v[74:77], v[232:235], v[166:169], v[74:77]
	v_mfma_f32_16x16x32_bf16 v[70:73], v[224:227], v[174:177], v[70:73]
	v_mfma_f32_16x16x32_bf16 v[66:69], v[232:235], v[174:177], v[66:69]
	s_mov_b32 m0, s52
	v_lshl_add_u64 v[188:189], v[206:207], 0, s[12:13]
	s_barrier
	ds_read_b128 v[146:149], v194 offset:49152
	ds_read_b128 v[150:153], v194 offset:50176
	ds_read_b128 v[154:157], v194 offset:51200
	ds_read_b128 v[158:161], v194 offset:52224
	ds_read_b128 v[162:165], v194 offset:53248
	ds_read_b128 v[166:169], v194 offset:54272
	ds_read_b128 v[170:173], v194 offset:55296
	ds_read_b128 v[174:177], v194 offset:56320
	global_load_lds_dwordx4 v[188:189], off
	v_lshl_add_u64 v[188:189], v[208:209], 0, s[12:13]
	s_mov_b32 m0, s53
	s_nop 0
	global_load_lds_dwordx4 v[188:189], off
	s_barrier
	s_waitcnt lgkmcnt(0)
	s_waitcnt lgkmcnt(0)
	v_mfma_f32_16x16x32_bf16 v[62:65], v[130:133], v[146:149], v[62:65]
	v_mfma_f32_16x16x32_bf16 v[58:61], v[138:141], v[146:149], v[58:61]
	v_mfma_f32_16x16x32_bf16 v[46:49], v[130:133], v[154:157], v[46:49]
	v_mfma_f32_16x16x32_bf16 v[42:45], v[138:141], v[154:157], v[42:45]
	v_mfma_f32_16x16x32_bf16 v[30:33], v[130:133], v[162:165], v[30:33]
	v_mfma_f32_16x16x32_bf16 v[26:29], v[138:141], v[162:165], v[26:29]
	v_mfma_f32_16x16x32_bf16 v[14:17], v[130:133], v[170:173], v[14:17]
	v_mfma_f32_16x16x32_bf16 v[10:13], v[138:141], v[170:173], v[10:13]
	v_mfma_f32_16x16x32_bf16 v[62:65], v[134:137], v[150:153], v[62:65]
	v_mfma_f32_16x16x32_bf16 v[58:61], v[142:145], v[150:153], v[58:61]
	v_mfma_f32_16x16x32_bf16 v[46:49], v[134:137], v[158:161], v[46:49]
	v_mfma_f32_16x16x32_bf16 v[42:45], v[142:145], v[158:161], v[42:45]
	v_mfma_f32_16x16x32_bf16 v[30:33], v[134:137], v[166:169], v[30:33]
	v_mfma_f32_16x16x32_bf16 v[26:29], v[142:145], v[166:169], v[26:29]
	v_mfma_f32_16x16x32_bf16 v[14:17], v[134:137], v[174:177], v[14:17]
	v_mfma_f32_16x16x32_bf16 v[10:13], v[142:145], v[174:177], v[10:13]
	s_barrier
	s_add_u32 s4, s4, 0x40080
	s_addc_u32 s5, s5, 0
	s_add_i32 s30, s31, s40
	v_lshl_add_u64 v[130:131], s[4:5], 0, v[178:179]
	s_mov_b32 m0, s30
	s_nop 0
	global_load_lds_dwordx4 v[130:131], off
	v_lshl_add_u64 v[130:131], s[4:5], 0, v[180:181]
	s_add_i32 m0, s30, 0x2000
	s_nop 0
	global_load_lds_dwordx4 v[130:131], off
	s_waitcnt vmcnt(6)
	s_barrier
	v_mfma_f32_16x16x32_bf16 v[54:57], v[196:199], v[146:149], v[54:57]
	v_mfma_f32_16x16x32_bf16 v[50:53], v[228:231], v[146:149], v[50:53]
	v_mfma_f32_16x16x32_bf16 v[38:41], v[196:199], v[154:157], v[38:41]
	v_mfma_f32_16x16x32_bf16 v[34:37], v[228:231], v[154:157], v[34:37]
	v_mfma_f32_16x16x32_bf16 v[22:25], v[196:199], v[162:165], v[22:25]
	v_mfma_f32_16x16x32_bf16 v[18:21], v[228:231], v[162:165], v[18:21]
	v_mfma_f32_16x16x32_bf16 v[6:9], v[196:199], v[170:173], v[6:9]
	v_mfma_f32_16x16x32_bf16 v[2:5], v[228:231], v[170:173], v[2:5]
	v_mfma_f32_16x16x32_bf16 v[54:57], v[224:227], v[150:153], v[54:57]
	v_mfma_f32_16x16x32_bf16 v[50:53], v[232:235], v[150:153], v[50:53]
	v_mfma_f32_16x16x32_bf16 v[38:41], v[224:227], v[158:161], v[38:41]
	v_mfma_f32_16x16x32_bf16 v[34:37], v[232:235], v[158:161], v[34:37]
	v_mfma_f32_16x16x32_bf16 v[22:25], v[224:227], v[166:169], v[22:25]
	v_mfma_f32_16x16x32_bf16 v[18:21], v[232:235], v[166:169], v[18:21]
	v_mfma_f32_16x16x32_bf16 v[6:9], v[224:227], v[174:177], v[6:9]
	v_mfma_f32_16x16x32_bf16 v[2:5], v[232:235], v[174:177], v[2:5]
	s_add_i32 s61, s61, 2
	s_cmp_gt_u32 s61, 13
	s_cbranch_scc1 .Lx_in
	s_barrier
	s_mov_b64 s[4:5], s[28:29]
	s_branch .LBB0_125
.Lx_in:
	s_cmp_lt_u32 s74, 0x100
	s_cbranch_scc0 .LBB0_130
	s_barrier
